# P0 gate fp6 loop: issue all 32 row loads back to back (the compiler waited on the first load alone); on top of hosted fp6 conversion in attention
# speedup vs baseline: 1.0271x; 1.0092x over previous
; template <int MODE>
; __device__ __forceinline__ void tr_matrix6(const float* W, int nb, int K, int N, unsigned char* WT, int drows, int rot, int gw, int NGW, int lane, float wscale) {
;     const int nbn = N / 32, per = (K / 256) * nbn, total = nb * per;
;     int it = gw - rot; if (it < 0) it += NGW;
;     const int c = lane & 7, q = lane >> 3;
;     for (; it < total; it += NGW) {
;         const int e = it / per, r = it - e * per, kb = r / nbn, nbk = r - kb * nbn, n0 = nbk * 32, k0 = kb * 256;
;         const float* src = W + (size_t)e * K * N + (size_t)(k0 + 32 * q) * N + n0 + 4 * c;
;         f32x4 v[32];
; #pragma unroll
;         for (int i = 0; i < 32; ++i) v[i] = *(const f32x4*)(src + (size_t)i * N);
.LBB0_56:
	s_mul_hi_i32 s6, s46, 0x92492493
	s_add_i32 s6, s6, s46
	s_lshr_b32 s7, s6, 31
	s_ashr_i32 s6, s6, 10
	s_add_i32 s6, s6, s7
	s_mul_i32 s7, s6, 0xfffff900
	s_mul_i32 s8, s6, 0x700
	s_mul_hi_i32 s9, s6, 0x3800000
	s_mul_i32 s10, s6, 0x3800000
	s_mul_hi_i32 s12, s6, 0x1c00000
	s_mul_i32 s13, s6, 0x1c00000
	s_add_i32 s6, s46, s7
	s_mul_hi_i32 s7, s6, 0x92492493
	s_add_i32 s7, s7, s6
	s_lshr_b32 s6, s7, 31
	s_ashr_i32 s7, s7, 7
	s_add_i32 s6, s7, s6
	s_mul_i32 s7, s6, 0xffffff20
	s_sub_i32 s7, s7, s8
	s_add_i32 s7, s46, s7
	s_lshl_b32 s6, s6, 8
	s_lshl_b32 s8, s7, 5
	s_add_u32 s10, s22, s10
	s_addc_u32 s11, s23, s9
	v_or_b32_e32 v4, s6, v146
	v_mov_b64_e32 v[2:3], s[10:11]
	s_ashr_i32 s9, s8, 31
	s_lshl_b32 s7, s7, 6
	v_mad_i64_i32 v[2:3], s[10:11], v4, s0, v[2:3]
	s_and_b32 s18, s8, 0x60
	s_and_b32 s7, s7, 0xffffff00
	v_lshl_add_u64 v[2:3], s[8:9], 2, v[2:3]
	s_add_u32 s10, s40, s13
	v_lshl_add_u64 v[8:9], v[2:3], 0, v[148:149]
	s_addc_u32 s11, s41, s12
	s_or_b32 s8, s7, s18
	v_add_co_u32_e32 v10, vcc, s0, v8
	v_or_b32_e32 v6, s8, v132
	s_nop 0
	v_addc_co_u32_e32 v11, vcc, 0, v9, vcc
	s_mov_b32 s8, 0xe000
	v_add_co_u32_e32 v12, vcc, s8, v8
	s_mov_b32 s8, 0x15000
	s_nop 0
	v_addc_co_u32_e32 v13, vcc, 0, v9, vcc
	v_add_co_u32_e32 v16, vcc, s8, v8
	s_mov_b32 s8, 0x1c000
	s_nop 0
	v_addc_co_u32_e32 v17, vcc, 0, v9, vcc
	v_add_co_u32_e32 v20, vcc, s8, v8
	s_mov_b32 s8, 0x23000
	s_nop 0
	v_addc_co_u32_e32 v21, vcc, 0, v9, vcc
	v_add_co_u32_e32 v24, vcc, s8, v8
	s_mov_b32 s8, 0x2a000
	s_nop 0
	v_addc_co_u32_e32 v25, vcc, 0, v9, vcc
	v_add_co_u32_e32 v28, vcc, s8, v8
	s_mov_b32 s8, 0x31000
	s_nop 0
	v_addc_co_u32_e32 v29, vcc, 0, v9, vcc
	v_add_co_u32_e32 v32, vcc, s8, v8
	s_mov_b32 s8, 0x38000
	s_nop 0
	v_addc_co_u32_e32 v33, vcc, 0, v9, vcc
	s_waitcnt vmcnt(15)
	v_add_co_u32_e32 v36, vcc, s8, v8
	s_mov_b32 s8, 0x3f000
	s_nop 0
	v_addc_co_u32_e32 v37, vcc, 0, v9, vcc
	s_waitcnt vmcnt(14)
	v_add_co_u32_e32 v40, vcc, s8, v8
	s_mov_b32 s8, 0x46000
	s_nop 0
	v_addc_co_u32_e32 v41, vcc, 0, v9, vcc
	s_waitcnt vmcnt(13)
	v_add_co_u32_e32 v44, vcc, s8, v8
	s_mov_b32 s8, 0x4d000
	s_nop 0
	v_addc_co_u32_e32 v45, vcc, 0, v9, vcc
	s_waitcnt vmcnt(12)
	v_add_co_u32_e32 v48, vcc, s8, v8
	s_mov_b32 s8, 0x54000
	s_nop 0
	v_addc_co_u32_e32 v49, vcc, 0, v9, vcc
	s_waitcnt vmcnt(7)
	v_add_co_u32_e32 v52, vcc, s8, v8
	s_mov_b32 s8, 0x5b000
	s_nop 0
	v_addc_co_u32_e32 v53, vcc, 0, v9, vcc
	s_waitcnt vmcnt(6)
	v_add_co_u32_e32 v56, vcc, s8, v8
	s_mov_b32 s8, 0x62000
	s_nop 0
	v_addc_co_u32_e32 v57, vcc, 0, v9, vcc
	s_waitcnt vmcnt(5)
	v_add_co_u32_e32 v60, vcc, s8, v8
	s_mov_b32 s8, 0x69000
	s_nop 0
	v_addc_co_u32_e32 v61, vcc, 0, v9, vcc
	s_waitcnt vmcnt(4)
	v_add_co_u32_e32 v64, vcc, s8, v8
	s_mov_b32 s8, 0x70000
	s_nop 0
	v_addc_co_u32_e32 v65, vcc, 0, v9, vcc
	v_add_co_u32_e32 v68, vcc, s8, v8
	s_mov_b32 s8, 0x77000
	s_nop 0
	v_addc_co_u32_e32 v69, vcc, 0, v9, vcc
	v_add_co_u32_e32 v72, vcc, s8, v8
	s_mov_b32 s8, 0x7e000
	s_nop 0
	v_addc_co_u32_e32 v73, vcc, 0, v9, vcc
	v_add_co_u32_e32 v76, vcc, s8, v8
	s_mov_b32 s8, 0x85000
	s_nop 0
	v_addc_co_u32_e32 v77, vcc, 0, v9, vcc
	v_add_co_u32_e32 v80, vcc, s8, v8
	s_mov_b32 s8, 0x8c000
	s_nop 0
	v_addc_co_u32_e32 v81, vcc, 0, v9, vcc
	v_add_co_u32_e32 v84, vcc, s8, v8
	global_load_dwordx4 v[2:5], v[8:9], off
	s_nop 0
	v_addc_co_u32_e32 v85, vcc, 0, v9, vcc
	v_add_co_u32_e32 v88, vcc, s1, v8
	v_ashrrev_i32_e32 v7, 31, v6
	s_nop 0
	v_addc_co_u32_e32 v89, vcc, 0, v9, vcc
	v_add_co_u32_e32 v92, vcc, s5, v8
	v_lshlrev_b64 v[6:7], 11, v[6:7]
	s_nop 0
	v_addc_co_u32_e32 v93, vcc, 0, v9, vcc
	v_add_co_u32_e32 v96, vcc, s14, v8
	s_ashr_i32 s7, s6, 31
	s_nop 0
	v_addc_co_u32_e32 v97, vcc, 0, v9, vcc
	v_add_co_u32_e32 v100, vcc, s15, v8
	v_lshl_add_u64 v[6:7], s[10:11], 0, v[6:7]
	s_nop 0
	v_addc_co_u32_e32 v101, vcc, 0, v9, vcc
	v_add_co_u32_e32 v104, vcc, s16, v8
	v_lshl_add_u64 v[6:7], v[6:7], 0, s[6:7]
	s_nop 0
	v_addc_co_u32_e32 v105, vcc, 0, v9, vcc
	v_add_co_u32_e32 v108, vcc, s17, v8
	v_lshl_add_u64 v[136:137], v[6:7], 0, v[146:147]
	s_nop 0
	v_addc_co_u32_e32 v109, vcc, 0, v9, vcc
	v_add_co_u32_e32 v112, vcc, s33, v8
	v_mov_b32_e32 v131, v130
	s_nop 0
	v_addc_co_u32_e32 v113, vcc, 0, v9, vcc
	v_add_co_u32_e32 v116, vcc, s38, v8
	s_add_i32 s46, s46, s72
	s_nop 0
	v_addc_co_u32_e32 v117, vcc, 0, v9, vcc
	v_add_co_u32_e32 v120, vcc, s39, v8
	s_cmpk_lt_i32 s46, 0x1c00
	s_nop 0
	v_addc_co_u32_e32 v121, vcc, 0, v9, vcc
	v_add_co_u32_e32 v124, vcc, s42, v8
	s_nop 1
	v_addc_co_u32_e32 v125, vcc, 0, v9, vcc
	v_add_co_u32_e32 v128, vcc, s43, v8
	s_nop 1
	v_addc_co_u32_e32 v129, vcc, 0, v9, vcc
	global_load_dwordx4 v[8:11], v[10:11], off
	s_nop 0
	global_load_dwordx4 v[12:15], v[12:13], off
	s_nop 0
	global_load_dwordx4 v[16:19], v[16:17], off
	s_nop 0
	global_load_dwordx4 v[20:23], v[20:21], off
	s_nop 0
	global_load_dwordx4 v[24:27], v[24:25], off
	s_nop 0
	global_load_dwordx4 v[28:31], v[28:29], off
	s_nop 0
	global_load_dwordx4 v[32:35], v[32:33], off
	s_nop 0
	global_load_dwordx4 v[36:39], v[36:37], off
	s_nop 0
	global_load_dwordx4 v[40:43], v[40:41], off
	s_nop 0
	global_load_dwordx4 v[44:47], v[44:45], off
	s_nop 0
	global_load_dwordx4 v[48:51], v[48:49], off
	s_nop 0
	global_load_dwordx4 v[52:55], v[52:53], off
	s_nop 0
	global_load_dwordx4 v[56:59], v[56:57], off
	s_nop 0
	global_load_dwordx4 v[60:63], v[60:61], off
	s_nop 0
	global_load_dwordx4 v[64:67], v[64:65], off
	s_nop 0
	global_load_dwordx4 v[68:71], v[68:69], off
	s_nop 0
	global_load_dwordx4 v[72:75], v[72:73], off
	s_nop 0
	global_load_dwordx4 v[76:79], v[76:77], off
	s_nop 0
	global_load_dwordx4 v[80:83], v[80:81], off
	s_nop 0
	global_load_dwordx4 v[84:87], v[84:85], off
	s_nop 0
	global_load_dwordx4 v[88:91], v[88:89], off
	s_nop 0
	global_load_dwordx4 v[92:95], v[92:93], off
	s_nop 0
	global_load_dwordx4 v[96:99], v[96:97], off
	s_nop 0
	global_load_dwordx4 v[100:103], v[100:101], off
	s_nop 0
	global_load_dwordx4 v[104:107], v[104:105], off
	s_nop 0
	global_load_dwordx4 v[108:111], v[108:109], off
	s_nop 0
	global_load_dwordx4 v[112:115], v[112:113], off
	s_nop 0
	global_load_dwordx4 v[116:119], v[116:117], off
	s_nop 0
	global_load_dwordx4 v[120:123], v[120:121], off
	s_nop 0
	global_load_dwordx4 v[124:127], v[124:125], off
	s_nop 0
	global_load_dwordx4 v[138:141], v[128:129], off
	s_waitcnt vmcnt(31)
; template <int MODE>
; __device__ __forceinline__ void tr_matrix6(const float* W, int nb, int K, int N, unsigned char* WT, int drows, int rot, int gw, int NGW, int lane, float wscale) {
;     ...
;         for (int j = 0; j < 4; ++j) { float x[32];
; #pragma unroll
;             for (int i = 0; i < 32; ++i) x[i] = v[i][j] * wscale;
;             const v6u w = pk32_fp6(x);
	v_mul_f32_e32 v2, 0x42b40000, v2
	v_mul_f32_e32 v3, 0x42b40000, v3
	v_mul_f32_e32 v4, 0x42b40000, v4
	v_mul_f32_e32 v5, 0x42b40000, v5
	v_med3_f32 v2, v2, s44, v133
	v_add_co_u32_e32 v134, vcc, s45, v136
	s_waitcnt vmcnt(30)
	v_mul_f32_e32 v6, 0x42b40000, v8
	v_mul_f32_e32 v128, 0x42b40000, v9
	v_mul_f32_e32 v129, 0x42b40000, v10
	v_mul_f32_e32 v142, 0x42b40000, v11
	s_waitcnt vmcnt(29)
	v_mul_f32_e32 v7, 0x42b40000, v12
	v_mul_f32_e32 v143, 0x42b40000, v13
	v_mul_f32_e32 v145, 0x42b40000, v14
	v_mul_f32_e32 v150, 0x42b40000, v15
	s_waitcnt vmcnt(28)
	v_mul_f32_e32 v8, 0x42b40000, v16
	v_mul_f32_e32 v151, 0x42b40000, v17
	s_waitcnt vmcnt(27)
	v_mul_f32_e32 v9, 0x42b40000, v20
	v_mul_f32_e32 v20, 0x42b40000, v22
	v_mul_f32_e32 v22, 0x42b40000, v23
	s_waitcnt vmcnt(26)
	v_mul_f32_e32 v10, 0x42b40000, v24
	v_mul_f32_e32 v23, 0x42b40000, v26
	v_mul_f32_e32 v24, 0x42b40000, v27
	s_waitcnt vmcnt(25)
	v_mul_f32_e32 v11, 0x42b40000, v28
	v_mul_f32_e32 v26, 0x42b40000, v30
	v_mul_f32_e32 v27, 0x42b40000, v31
	s_waitcnt vmcnt(24)
	v_mul_f32_e32 v12, 0x42b40000, v32
	v_mul_f32_e32 v28, 0x42b40000, v33
	v_mul_f32_e32 v30, 0x42b40000, v35
	s_waitcnt vmcnt(23)
	v_mul_f32_e32 v13, 0x42b40000, v36
	v_mul_f32_e32 v31, 0x42b40000, v37
	v_mul_f32_e32 v32, 0x42b40000, v38
	v_mul_f32_e32 v33, 0x42b40000, v39
	s_waitcnt vmcnt(22)
	v_mul_f32_e32 v14, 0x42b40000, v40
	v_mul_f32_e32 v35, 0x42b40000, v41
	v_mul_f32_e32 v155, 0x42b40000, v42
	v_mul_f32_e32 v156, 0x42b40000, v43
	s_waitcnt vmcnt(21)
	v_mul_f32_e32 v15, 0x42b40000, v44
	v_mul_f32_e32 v157, 0x42b40000, v47
	s_waitcnt vmcnt(20)
	v_mul_f32_e32 v16, 0x42b40000, v48
	v_mul_f32_e32 v37, 0x42b40000, v49
	v_mul_f32_e32 v158, 0x42b40000, v51
	s_waitcnt vmcnt(19)
	v_mul_f32_e32 v17, 0x42b40000, v52
	v_mul_f32_e32 v38, 0x42b40000, v53
	v_mul_f32_e32 v159, 0x42b40000, v55
	s_waitcnt vmcnt(18)
	v_mul_f32_e32 v39, 0x42b40000, v56
	v_mul_f32_e32 v40, 0x42b40000, v57
	v_mul_f32_e32 v47, 0x42b40000, v58
	v_mul_f32_e32 v160, 0x42b40000, v59
	s_waitcnt vmcnt(17)
	v_mul_f32_e32 v41, 0x42b40000, v60
	v_mul_f32_e32 v42, 0x42b40000, v61
	v_mul_f32_e32 v161, 0x42b40000, v63
	s_waitcnt vmcnt(16)
	v_mul_f32_e32 v43, 0x42b40000, v64
	v_mul_f32_e32 v49, 0x42b40000, v65
	s_waitcnt vmcnt(15)
	v_mul_f32_e32 v51, 0x42b40000, v68
	s_waitcnt vmcnt(14)
	v_mul_f32_e32 v53, 0x42b40000, v72
	v_mul_f32_e32 v166, 0x42b40000, v74
	v_mul_f32_e32 v167, 0x42b40000, v75
	s_waitcnt vmcnt(13)
	v_mul_f32_e32 v55, 0x42b40000, v76
	v_mul_f32_e32 v56, 0x42b40000, v77
	v_mul_f32_e32 v168, 0x42b40000, v78
	v_mul_f32_e32 v169, 0x42b40000, v79
	s_waitcnt vmcnt(12)
	v_mul_f32_e32 v57, 0x42b40000, v80
	v_mul_f32_e32 v58, 0x42b40000, v81
	s_waitcnt vmcnt(11)
	v_mul_f32_e32 v59, 0x42b40000, v84
	s_waitcnt vmcnt(10)
	v_mul_f32_e32 v61, 0x42b40000, v88
	s_waitcnt vmcnt(9)
	v_mul_f32_e32 v63, 0x42b40000, v92
	s_waitcnt vmcnt(8)
	v_mul_f32_e32 v65, 0x42b40000, v96
	s_waitcnt vmcnt(7)
	v_mul_f32_e32 v74, 0x42b40000, v100
	s_waitcnt vmcnt(6)
	v_mul_f32_e32 v75, 0x42b40000, v104
	s_waitcnt vmcnt(5)
	v_mul_f32_e32 v76, 0x42b40000, v108
	s_waitcnt vmcnt(4)
	v_mul_f32_e32 v77, 0x42b40000, v112
	s_waitcnt vmcnt(3)
	v_mul_f32_e32 v78, 0x42b40000, v116
	s_waitcnt vmcnt(2)
	v_mul_f32_e32 v79, 0x42b40000, v120
	s_waitcnt vmcnt(1)
	v_mul_f32_e32 v80, 0x42b40000, v124
	s_waitcnt vmcnt(0)
	v_mul_f32_e32 v81, 0x42b40000, v138
	v_mul_f32_e32 v152, 0x42b40000, v18
	v_mul_f32_e32 v153, 0x42b40000, v19
	v_mul_f32_e32 v19, 0x42b40000, v21
	v_mul_f32_e32 v21, 0x42b40000, v25
	v_mul_f32_e32 v25, 0x42b40000, v29
	v_mul_f32_e32 v29, 0x42b40000, v34
	v_mul_f32_e32 v36, 0x42b40000, v45
	v_mul_f32_e32 v44, 0x42b40000, v46
	v_mul_f32_e32 v45, 0x42b40000, v50
	v_mul_f32_e32 v46, 0x42b40000, v54
	v_mul_f32_e32 v48, 0x42b40000, v62
	v_mul_f32_e32 v162, 0x42b40000, v66
	v_mul_f32_e32 v163, 0x42b40000, v67
	v_mul_f32_e32 v52, 0x42b40000, v69
	v_mul_f32_e32 v164, 0x42b40000, v70
	v_mul_f32_e32 v165, 0x42b40000, v71
	v_mul_f32_e32 v54, 0x42b40000, v73
	v_mul_f32_e32 v171, 0x42b40000, v83
	v_mul_f32_e32 v60, 0x42b40000, v85
	v_mul_f32_e32 v173, 0x42b40000, v87
	v_mul_f32_e32 v62, 0x42b40000, v89
	v_mul_f32_e32 v174, 0x42b40000, v90
	v_mul_f32_e32 v175, 0x42b40000, v91
	v_mul_f32_e32 v64, 0x42b40000, v93
	v_mul_f32_e32 v176, 0x42b40000, v94
	v_mul_f32_e32 v177, 0x42b40000, v95
	v_mul_f32_e32 v89, 0x42b40000, v97
	v_mul_f32_e32 v179, 0x42b40000, v99
	v_mul_f32_e32 v90, 0x42b40000, v101
	v_mul_f32_e32 v181, 0x42b40000, v103
	v_mul_f32_e32 v91, 0x42b40000, v105
	v_mul_f32_e32 v183, 0x42b40000, v107
	v_mul_f32_e32 v92, 0x42b40000, v109
	v_mul_f32_e32 v184, 0x42b40000, v111
	v_mul_f32_e32 v93, 0x42b40000, v113
	v_mul_f32_e32 v185, 0x42b40000, v115
	v_mul_f32_e32 v94, 0x42b40000, v117
	v_mul_f32_e32 v186, 0x42b40000, v119
	v_mul_f32_e32 v95, 0x42b40000, v121
	v_mul_f32_e32 v187, 0x42b40000, v123
	v_mul_f32_e32 v96, 0x42b40000, v125
	v_mul_f32_e32 v188, 0x42b40000, v127
	v_mul_f32_e32 v97, 0x42b40000, v139
	v_mul_f32_e32 v138, 0x42b40000, v141
	v_med3_f32 v50, v3, s44, v133
	v_med3_f32 v34, v4, s44, v133
	v_med3_f32 v18, v5, s44, v133
	v_med3_f32 v3, v6, s44, v133
	v_med3_f32 v66, v51, s44, v133
	v_med3_f32 v67, v53, s44, v133
	v_med3_f32 v4, v7, s44, v133
	v_med3_f32 v68, v55, s44, v133
	v_med3_f32 v5, v8, s44, v133
	v_med3_f32 v69, v57, s44, v133
	v_med3_f32 v6, v9, s44, v133
	v_med3_f32 v70, v59, s44, v133
	v_med3_f32 v7, v10, s44, v133
	v_med3_f32 v71, v61, s44, v133
	v_med3_f32 v8, v11, s44, v133
	v_med3_f32 v72, v63, s44, v133
	v_med3_f32 v9, v12, s44, v133
; __device__ __forceinline__ v6u pk32_fp6(const float (&x)[32]) {
;     ...
;     for (int i = 0; i < 16; ++i) { a[i] = __builtin_amdgcn_fmed3f(x[i], -7.5f, 7.5f); b[i] = __builtin_amdgcn_fmed3f(x[16 + i], -7.5f, 7.5f); }
;     return __builtin_amdgcn_cvt_scalef32_2xpk16_fp6_f32(a, b, 1.0f);
; template <int MODE>
; __device__ __forceinline__ void tr_matrix6(const float* W, int nb, int K, int N, unsigned char* WT, int drows, int rot, int gw, int NGW, int lane, float wscale) {
;     ...
;         for (int j = 0; j < 4; ++j) { float x[32];
; #pragma unroll
;             for (int i = 0; i < 32; ++i) x[i] = v[i][j] * wscale;
;             const v6u w = pk32_fp6(x);
;             *(u32x4*)(dst + (size_t)j * K) = (u32x4){w[0], w[1], w[2], w[3]}; *(u32x4*)(dst + (size_t)j * K + 16) = (u32x4){w[4], w[5], 0u, 0u}; }
;     }
	v_med3_f32 v73, v65, s44, v133
	v_med3_f32 v10, v13, s44, v133
	v_med3_f32 v74, v74, s44, v133
	v_med3_f32 v11, v14, s44, v133
	v_med3_f32 v75, v75, s44, v133
	v_med3_f32 v12, v15, s44, v133
	v_med3_f32 v76, v76, s44, v133
	v_med3_f32 v13, v16, s44, v133
	v_med3_f32 v77, v77, s44, v133
	v_med3_f32 v14, v17, s44, v133
	v_med3_f32 v78, v78, s44, v133
	v_med3_f32 v15, v39, s44, v133
	v_med3_f32 v79, v79, s44, v133
	v_med3_f32 v16, v41, s44, v133
	v_med3_f32 v80, v80, s44, v133
	v_med3_f32 v17, v43, s44, v133
	v_med3_f32 v81, v81, s44, v133
	v_mul_f32_e32 v170, 0x42b40000, v82
	v_mul_f32_e32 v172, 0x42b40000, v86
	v_mul_f32_e32 v178, 0x42b40000, v98
	v_mul_f32_e32 v180, 0x42b40000, v102
	v_mul_f32_e32 v182, 0x42b40000, v106
	v_mul_f32_e32 v108, 0x42b40000, v110
	v_mul_f32_e32 v109, 0x42b40000, v114
	v_mul_f32_e32 v110, 0x42b40000, v118
	v_mul_f32_e32 v111, 0x42b40000, v122
	v_mul_f32_e32 v112, 0x42b40000, v126
	v_mul_f32_e32 v113, 0x42b40000, v140
	v_med3_f32 v51, v128, s44, v133
	v_med3_f32 v82, v52, s44, v133
	v_med3_f32 v83, v54, s44, v133
	v_med3_f32 v52, v143, s44, v133
	v_med3_f32 v84, v56, s44, v133
	v_med3_f32 v53, v151, s44, v133
	v_med3_f32 v85, v58, s44, v133
	v_med3_f32 v54, v19, s44, v133
	v_med3_f32 v86, v60, s44, v133
	v_med3_f32 v55, v21, s44, v133
	v_med3_f32 v87, v62, s44, v133
	v_med3_f32 v56, v25, s44, v133
	v_med3_f32 v88, v64, s44, v133
	v_med3_f32 v57, v28, s44, v133
	v_med3_f32 v89, v89, s44, v133
	v_med3_f32 v58, v31, s44, v133
	v_med3_f32 v90, v90, s44, v133
	v_med3_f32 v59, v35, s44, v133
	v_med3_f32 v91, v91, s44, v133
	v_med3_f32 v60, v36, s44, v133
	v_med3_f32 v92, v92, s44, v133
	v_med3_f32 v61, v37, s44, v133
	v_med3_f32 v93, v93, s44, v133
	v_med3_f32 v62, v38, s44, v133
	v_med3_f32 v94, v94, s44, v133
	v_med3_f32 v63, v40, s44, v133
	v_med3_f32 v95, v95, s44, v133
	v_med3_f32 v64, v42, s44, v133
	v_med3_f32 v96, v96, s44, v133
	v_med3_f32 v65, v49, s44, v133
	v_med3_f32 v97, v97, s44, v133
	v_med3_f32 v35, v129, s44, v133
	v_med3_f32 v38, v20, s44, v133
	v_med3_f32 v39, v23, s44, v133
	v_med3_f32 v40, v26, s44, v133
	v_med3_f32 v41, v29, s44, v133
	v_med3_f32 v42, v32, s44, v133
	v_med3_f32 v19, v142, s44, v133
	v_med3_f32 v114, v165, s44, v133
	v_med3_f32 v115, v167, s44, v133
	v_med3_f32 v20, v150, s44, v133
	v_med3_f32 v116, v169, s44, v133
	v_med3_f32 v21, v153, s44, v133
	v_med3_f32 v117, v171, s44, v133
	v_med3_f32 v22, v22, s44, v133
	v_med3_f32 v118, v173, s44, v133
	v_med3_f32 v23, v24, s44, v133
	v_med3_f32 v119, v175, s44, v133
	v_med3_f32 v24, v27, s44, v133
	v_med3_f32 v120, v177, s44, v133
	v_med3_f32 v25, v30, s44, v133
	v_med3_f32 v121, v179, s44, v133
	v_med3_f32 v26, v33, s44, v133
	v_med3_f32 v122, v181, s44, v133
	v_med3_f32 v27, v156, s44, v133
	v_med3_f32 v123, v183, s44, v133
	v_med3_f32 v28, v157, s44, v133
	v_med3_f32 v124, v184, s44, v133
	v_med3_f32 v29, v158, s44, v133
	v_med3_f32 v125, v185, s44, v133
	v_med3_f32 v30, v159, s44, v133
	v_med3_f32 v126, v186, s44, v133
	v_med3_f32 v31, v160, s44, v133
	v_med3_f32 v127, v187, s44, v133
	v_med3_f32 v32, v161, s44, v133
	v_med3_f32 v128, v188, s44, v133
	v_med3_f32 v33, v163, s44, v133
	v_med3_f32 v129, v138, s44, v133
	v_cvt_scalef32_2xpk16_fp6_f32 v[2:7], v[2:17], v[66:81], 1.0
	v_med3_f32 v98, v164, s44, v133
	v_med3_f32 v99, v166, s44, v133
	v_med3_f32 v36, v145, s44, v133
	v_med3_f32 v100, v168, s44, v133
	v_med3_f32 v37, v152, s44, v133
	v_med3_f32 v101, v170, s44, v133
	v_med3_f32 v102, v172, s44, v133
	v_med3_f32 v103, v174, s44, v133
	v_med3_f32 v104, v176, s44, v133
	v_med3_f32 v105, v178, s44, v133
	v_med3_f32 v106, v180, s44, v133
	v_med3_f32 v43, v155, s44, v133
	v_med3_f32 v107, v182, s44, v133
	v_med3_f32 v44, v44, s44, v133
	v_med3_f32 v108, v108, s44, v133
	v_med3_f32 v45, v45, s44, v133
	v_med3_f32 v109, v109, s44, v133
	v_med3_f32 v46, v46, s44, v133
	v_med3_f32 v110, v110, s44, v133
	v_med3_f32 v47, v47, s44, v133
	v_med3_f32 v111, v111, s44, v133
	v_med3_f32 v48, v48, s44, v133
	v_med3_f32 v112, v112, s44, v133
	v_med3_f32 v49, v162, s44, v133
	v_med3_f32 v113, v113, s44, v133
	v_cvt_scalef32_2xpk16_fp6_f32 v[8:13], v[50:65], v[82:97], 1.0
	v_cvt_scalef32_2xpk16_fp6_f32 v[14:19], v[18:33], v[114:129], 1.0
	v_mov_b32_e32 v128, v6
	v_mov_b32_e32 v129, v7
	v_addc_co_u32_e32 v135, vcc, 0, v137, vcc
	v_cvt_scalef32_2xpk16_fp6_f32 v[34:39], v[34:49], v[98:113], 1.0
	global_store_dwordx4 v[136:137], v[2:5], off
	global_store_dwordx4 v[136:137], v[8:11], off offset:2048
	global_store_dwordx4 v[134:135], v[34:37], off
	global_store_dwordx4 v[134:135], v[14:17], off offset:2048
	global_store_dwordx4 v[136:137], v[128:131], off offset:16
	s_nop 1
	v_mov_b32_e32 v128, v12
	v_mov_b32_e32 v129, v13
	global_store_dwordx4 v[136:137], v[128:131], off offset:2064
	s_nop 1
	v_mov_b32_e32 v128, v38
	v_mov_b32_e32 v129, v39
	global_store_dwordx4 v[134:135], v[128:131], off offset:16
	s_nop 1
	v_mov_b32_e32 v128, v18
	v_mov_b32_e32 v129, v19
	global_store_dwordx4 v[134:135], v[128:131], off offset:2064
	s_cbranch_scc1 .LBB0_56
	v_or_b32_e32 v145, 0x80, v132
	s_movk_i32 s0, 0x7000
	v_mov_b32_e32 v149, 0
	s_mov_b32 s1, 0x7e000
	s_mov_b32 s5, 0x85000
	s_mov_b32 s14, 0x8c000
	s_mov_b32 s15, 0x93000
	s_mov_b32 s16, 0x9a000
	s_mov_b32 s17, 0xa1000
	s_mov_b32 s22, 0xa8000
	s_mov_b32 s23, 0xaf000
	s_mov_b32 s33, 0xb6000
	s_mov_b32 s38, 0xbd000
	s_mov_b32 s39, 0xc4000
	s_mov_b32 s42, 0xcb000
	s_mov_b32 s43, 0xd2000
	s_mov_b32 s44, 0xd9000
	s_mov_b32 s45, 0xc0f00000
	s_movk_i32 s46, 0x1000
	v_mov_b32_e32 v155, 0x40f00000
